# main: q.bk term (tq) computed in phase 0 from register-resident x rows + DPP reduce, removing 16 u loads and 64-FMA chain from phase 2
# speedup vs baseline: 1.0199x; 1.0146x over previous
_Z7na_mainPKDF16_PKhS0_PKfS4_S4_S4_Pf:
	s_lshl_b32 s3, s2, 5
	s_and_b32 s3, s3, 0xe0
	s_ashr_i32 s2, s2, 3
	s_add_i32 s3, s3, s2
	s_ashr_i32 s2, s3, 6
	s_lshl_b32 s3, s3, 5
	s_and_b32 s14, s3, 0x7e0
	v_mov_b32_e32 v1, 0x7c0
	s_load_dwordx8 s[4:11], s[0:1], 0x0
	s_load_dwordx2 s[18:19], s[0:1], 0x20
	v_med3_u32 v1, s14, 32, v1
	v_subrev_u32_e32 v97, 32, v1
	s_ashr_i32 s3, s2, 31
	v_lshlrev_b32_e32 v58, 1, v97
	s_lshl_b64 s[12:13], s[2:3], 12
	v_mov_b32_e32 v59, 0
	v_sub_u32_e32 v60, s14, v97
	v_lshl_add_u64 v[10:11], s[12:13], 0, v[58:59]
	v_lshlrev_b64 v[2:3], 9, v[10:11]
	v_lshl_or_b32 v22, v60, 6, v0
	s_waitcnt lgkmcnt(0)
	v_and_b32_e32 v208, 31, v0
	v_lshlrev_b32_e32 v208, 5, v208
	global_load_dwordx4 v[192:195], v208, s[18:19]
	global_load_dwordx4 v[196:199], v208, s[18:19] offset:16
	v_lshl_add_u64 v[20:21], s[4:5], 0, v[2:3]
	v_ashrrev_i32_e32 v23, 31, v22
	v_lshl_add_u64 v[2:3], v[22:23], 4, v[20:21]
	global_load_dwordx4 v[12:15], v[2:3], off
	v_or_b32_e32 v28, 0x200, v22
	v_ashrrev_i32_e32 v29, 31, v28
	v_lshl_add_u64 v[2:3], v[28:29], 4, v[20:21]
	global_load_dwordx4 v[16:19], v[2:3], off
	v_or_b32_e32 v184, 0x400, v22
	v_ashrrev_i32_e32 v185, 31, v184
	v_lshl_add_u64 v[184:185], v[184:185], 4, v[20:21]
	v_or_b32_e32 v188, 0x600, v22
	v_ashrrev_i32_e32 v189, 31, v188
	v_lshl_add_u64 v[188:189], v[188:189], 4, v[20:21]
	global_load_dwordx4 v[184:187], v[184:185], off
	global_load_dwordx4 v[188:191], v[188:189], off
	v_lshrrev_b32_e32 v99, 6, v0
	v_and_b32_e32 v98, 63, v0
	v_lshlrev_b32_e32 v118, 13, v99
	v_lshl_or_b32 v58, v98, 5, v118
	s_movk_i32 s15, 0x1000
	v_lshl_add_u64 v[24:25], s[6:7], 0, v[58:59]
	v_or_b32_e32 v32, 0x400, v22
	v_or_b32_e32 v62, 0x600, v22
	v_add_co_u32_e32 v64, vcc, s15, v24
	s_mov_b64 s[12:13], 0x1000
	s_mov_b64 s[16:17], 0x1800
	v_lshlrev_b32_e32 v72, 1, v60
	v_lshrrev_b32_e32 v23, 5, v22
	v_and_b32_e32 v34, 32, v22
	v_ashrrev_i32_e32 v33, 31, v32
	v_ashrrev_i32_e32 v63, 31, v62
	v_addc_co_u32_e32 v65, vcc, 0, v25, vcc
	global_load_dwordx4 v[6:9], v58, s[6:7] offset:16
	global_load_dwordx4 v[2:5], v58, s[6:7]
	global_load_dwordx4 v[54:57], v58, s[6:7] offset:2064
	global_load_dwordx4 v[50:53], v58, s[6:7] offset:2048
	v_lshrrev_b32_e32 v58, 6, v22
	v_bfe_u32 v73, v22, 8, 2
	v_lshl_add_u64 v[26:27], v[24:25], 0, s[12:13]
	v_lshl_add_u64 v[24:25], v[24:25], 0, s[16:17]
	v_cmp_ne_u32_e32 vcc, 0, v34
	v_sub_u32_e32 v75, v23, v72
	global_load_dwordx4 v[42:45], v[64:65], off
	global_load_dwordx4 v[46:49], v[26:27], off offset:16
	global_load_dwordx4 v[34:37], v[64:65], off offset:2048
	global_load_dwordx4 v[38:41], v[24:25], off offset:16
	v_mov_b32_e32 v61, 0x60
	v_cndmask_b32_e32 v74, 0, v61, vcc
	v_add_u32_e32 v33, v74, v58
	v_lshlrev_b32_e32 v64, 2, v33
	v_bfe_u32 v96, v0, 4, 1
	v_and_b32_e32 v100, 15, v0
	v_mov_b32_e32 v30, v59
	v_mov_b32_e32 v31, v59
	v_and_b32_e32 v64, 12, v64
	v_mul_u32_u24_e32 v29, 0xc000, v96
	v_bitop3_b32 v64, v64, v100, v73 bitop3:0x36
	v_lshl_or_b32 v64, v64, 4, v29
	v_lshlrev_b32_e32 v63, 1, v75
	v_lshl_add_u32 v33, v33, 8, v64
	v_bfe_u32 v71, v0, 1, 4
	v_and_b32_e32 v70, 32, v0
	v_lshlrev_b32_e32 v1, 3, v0
	v_lshrrev_b32_e32 v58, 1, v75
	v_and_b32_e32 v1, 8, v1
	v_add_lshl_u32 v58, v58, v70, 8
	v_lshlrev_b32_e32 v121, 3, v99
	v_bfe_u32 v101, v0, 4, 2
	v_lshlrev_b32_e32 v102, 2, v101
	v_and_b32_e32 v116, 31, v0
	v_bfe_u32 v119, v0, 5, 1
	v_lshlrev_b32_e32 v124, 1, v119
	v_lshlrev_b32_e32 v117, 8, v116
	v_lshrrev_b32_e32 v95, 4, v0
	s_movk_i32 s16, 0x60
	s_mov_b32 s17, 0xc000
	s_waitcnt vmcnt(11)
	v_fma_mix_f32 v200, v192, v12, 0 op_sel_hi:[0,1,0]
	v_fma_mix_f32 v201, v193, v12, 0 op_sel:[0,1,0] op_sel_hi:[0,1,0]
	v_fma_mix_f32 v200, v194, v13, v200 op_sel_hi:[0,1,0]
	v_fma_mix_f32 v201, v195, v13, v201 op_sel:[0,1,0] op_sel_hi:[0,1,0]
	v_fma_mix_f32 v200, v196, v14, v200 op_sel_hi:[0,1,0]
	v_fma_mix_f32 v201, v197, v14, v201 op_sel:[0,1,0] op_sel_hi:[0,1,0]
	v_fma_mix_f32 v200, v198, v15, v200 op_sel_hi:[0,1,0]
	v_fma_mix_f32 v201, v199, v15, v201 op_sel:[0,1,0] op_sel_hi:[0,1,0]
	v_cvt_f32_f16_e32 v65, v12
	v_cvt_f32_f16_sdwa v66, v12 dst_sel:DWORD dst_unused:UNUSED_PAD src0_sel:WORD_1
	v_cvt_f32_f16_e32 v69, v14
	v_cvt_f32_f16_sdwa v74, v14 dst_sel:DWORD dst_unused:UNUSED_PAD src0_sel:WORD_1
	v_cvt_f32_f16_e32 v67, v13
	v_cvt_f32_f16_sdwa v68, v13 dst_sel:DWORD dst_unused:UNUSED_PAD src0_sel:WORD_1
	v_cvt_f32_f16_e32 v76, v15
	v_cvt_f32_f16_sdwa v77, v15 dst_sel:DWORD dst_unused:UNUSED_PAD src0_sel:WORD_1
	v_cvt_pk_fp8_f32 v30, v65, v66
	v_cvt_pk_fp8_f32 v31, v69, v74
	ds_write_b128 v33, v[12:15]
	v_and_b32_e32 v12, 12, v63
	v_bfe_u32 v13, v75, 3, 2
	v_cvt_pk_fp8_f32 v30, v67, v68 op_sel:[0,0,1]
	v_cvt_pk_fp8_f32 v31, v76, v77 op_sel:[0,0,1]
	v_bitop3_b32 v12, v12, v71, v13 bitop3:0x36
	v_lshlrev_b32_e32 v12, 4, v12
	v_or3_b32 v12, v58, v12, v1
	v_add_u32_e32 v12, 0x23800, v12
	ds_write_b64 v12, v[30:31]
	v_and_b32_e32 v12, 32, v28
	v_cmp_ne_u32_e32 vcc, 0, v12
	v_lshrrev_b32_e32 v13, 6, v28
	v_bfe_u32 v15, v28, 8, 2
	v_cndmask_b32_e32 v12, 0, v61, vcc
	v_add_u32_e32 v12, v12, v13
	v_lshlrev_b32_e32 v13, 2, v12
	v_and_b32_e32 v13, 12, v13
	v_bitop3_b32 v13, v13, v100, v15 bitop3:0x36
	v_lshl_or_b32 v13, v13, 4, v29
	v_lshl_add_u32 v12, v12, 8, v13
	s_waitcnt vmcnt(10)
	v_fma_mix_f32 v202, v192, v16, 0 op_sel_hi:[0,1,0]
	v_fma_mix_f32 v203, v193, v16, 0 op_sel:[0,1,0] op_sel_hi:[0,1,0]
	v_fma_mix_f32 v202, v194, v17, v202 op_sel_hi:[0,1,0]
	v_fma_mix_f32 v203, v195, v17, v203 op_sel:[0,1,0] op_sel_hi:[0,1,0]
	v_fma_mix_f32 v202, v196, v18, v202 op_sel_hi:[0,1,0]
	v_fma_mix_f32 v203, v197, v18, v203 op_sel:[0,1,0] op_sel_hi:[0,1,0]
	v_fma_mix_f32 v202, v198, v19, v202 op_sel_hi:[0,1,0]
	v_fma_mix_f32 v203, v199, v19, v203 op_sel:[0,1,0] op_sel_hi:[0,1,0]
	v_cvt_f32_f16_e32 v13, v16
	v_cvt_f32_f16_sdwa v15, v16 dst_sel:DWORD dst_unused:UNUSED_PAD src0_sel:WORD_1
	ds_write_b128 v12, v[16:19]
	v_mov_b32_e32 v12, v59
	v_cvt_f32_f16_e32 v16, v17
	v_cvt_pk_fp8_f32 v12, v13, v15
	v_cvt_f32_f16_e32 v15, v18
	v_cvt_f32_f16_sdwa v18, v18 dst_sel:DWORD dst_unused:UNUSED_PAD src0_sel:WORD_1
	v_cvt_f32_f16_sdwa v17, v17 dst_sel:DWORD dst_unused:UNUSED_PAD src0_sel:WORD_1
	v_mov_b32_e32 v13, v59
	v_lshrrev_b32_e32 v14, 5, v28
	v_cvt_f32_f16_e32 v28, v19
	v_cvt_f32_f16_sdwa v19, v19 dst_sel:DWORD dst_unused:UNUSED_PAD src0_sel:WORD_1
	v_cvt_pk_fp8_f32 v13, v15, v18
	v_sub_u32_e32 v14, v14, v72
	v_cvt_pk_fp8_f32 v12, v16, v17 op_sel:[0,0,1]
	v_lshlrev_b32_e32 v16, 1, v14
	v_lshrrev_b32_e32 v15, 1, v14
	v_and_b32_e32 v16, 12, v16
	v_bfe_u32 v14, v14, 3, 2
	v_cvt_pk_fp8_f32 v13, v28, v19 op_sel:[0,0,1]
	v_bitop3_b32 v14, v16, v71, v14 bitop3:0x36
	v_add_lshl_u32 v15, v15, v70, 8
	v_lshlrev_b32_e32 v14, 4, v14
	v_or3_b32 v14, v15, v14, v1
	v_add_u32_e32 v14, 0x23800, v14
	ds_write_b64 v14, v[12:13]
	v_and_b32_e32 v12, 32, v32
	v_cmp_ne_u32_e32 vcc, 0, v12
	v_lshrrev_b32_e32 v13, 6, v32
	s_waitcnt vmcnt(9)
	v_fma_mix_f32 v204, v192, v184, 0 op_sel_hi:[0,1,0]
	v_fma_mix_f32 v205, v193, v184, 0 op_sel:[0,1,0] op_sel_hi:[0,1,0]
	v_fma_mix_f32 v204, v194, v185, v204 op_sel_hi:[0,1,0]
	v_fma_mix_f32 v205, v195, v185, v205 op_sel:[0,1,0] op_sel_hi:[0,1,0]
	v_fma_mix_f32 v204, v196, v186, v204 op_sel_hi:[0,1,0]
	v_fma_mix_f32 v205, v197, v186, v205 op_sel:[0,1,0] op_sel_hi:[0,1,0]
	v_fma_mix_f32 v204, v198, v187, v204 op_sel_hi:[0,1,0]
	v_fma_mix_f32 v205, v199, v187, v205 op_sel:[0,1,0] op_sel_hi:[0,1,0]
	v_cvt_f32_f16_sdwa v15, v184 dst_sel:DWORD dst_unused:UNUSED_PAD src0_sel:WORD_1
	v_cndmask_b32_e32 v12, 0, v61, vcc
	v_add_u32_e32 v12, v12, v13
	v_lshlrev_b32_e32 v13, 2, v12
	v_and_b32_e32 v13, 12, v13
	v_bitop3_b32 v13, v13, v100, v73 bitop3:0x36
	v_lshl_or_b32 v13, v13, 4, v29
	v_lshl_add_u32 v12, v12, 8, v13
	v_cvt_f32_f16_e32 v13, v184
	ds_write_b128 v12, v[184:187]
	v_mov_b32_e32 v12, v59
	v_cvt_f32_f16_sdwa v18, v186 dst_sel:DWORD dst_unused:UNUSED_PAD src0_sel:WORD_1
	v_cvt_pk_fp8_f32 v12, v13, v15
	v_cvt_f32_f16_e32 v15, v186
	v_cvt_f32_f16_e32 v16, v185
	v_cvt_f32_f16_sdwa v17, v185 dst_sel:DWORD dst_unused:UNUSED_PAD src0_sel:WORD_1
	v_mov_b32_e32 v13, v59
	v_lshrrev_b32_e32 v14, 5, v32
	v_cvt_f32_f16_e32 v19, v187
	v_cvt_f32_f16_sdwa v20, v187 dst_sel:DWORD dst_unused:UNUSED_PAD src0_sel:WORD_1
	v_cvt_pk_fp8_f32 v13, v15, v18
	v_sub_u32_e32 v14, v14, v72
	v_cvt_pk_fp8_f32 v12, v16, v17 op_sel:[0,0,1]
	v_lshlrev_b32_e32 v16, 1, v14
	v_lshrrev_b32_e32 v15, 1, v14
	v_and_b32_e32 v16, 12, v16
	v_bfe_u32 v14, v14, 3, 2
	v_cvt_pk_fp8_f32 v13, v19, v20 op_sel:[0,0,1]
	v_bitop3_b32 v14, v16, v71, v14 bitop3:0x36
	v_add_lshl_u32 v15, v15, v70, 8
	v_lshlrev_b32_e32 v14, 4, v14
	v_or3_b32 v14, v15, v14, v1
	v_add_u32_e32 v14, 0x23800, v14
	ds_write_b64 v14, v[12:13]
	v_and_b32_e32 v12, 32, v62
	v_cmp_ne_u32_e32 vcc, 0, v12
	v_lshrrev_b32_e32 v13, 6, v62
	v_bfe_u32 v15, v62, 8, 2
	v_cndmask_b32_e32 v12, 0, v61, vcc
	v_add_u32_e32 v12, v12, v13
	v_lshlrev_b32_e32 v13, 2, v12
	v_and_b32_e32 v13, 12, v13
	v_bitop3_b32 v13, v13, v100, v15 bitop3:0x36
	v_lshl_or_b32 v13, v13, 4, v29
	v_lshl_add_u32 v12, v12, 8, v13
	s_waitcnt vmcnt(8)
	v_fma_mix_f32 v206, v192, v188, 0 op_sel_hi:[0,1,0]
	v_fma_mix_f32 v207, v193, v188, 0 op_sel:[0,1,0] op_sel_hi:[0,1,0]
	v_fma_mix_f32 v206, v194, v189, v206 op_sel_hi:[0,1,0]
	v_fma_mix_f32 v207, v195, v189, v207 op_sel:[0,1,0] op_sel_hi:[0,1,0]
	v_fma_mix_f32 v206, v196, v190, v206 op_sel_hi:[0,1,0]
	v_fma_mix_f32 v207, v197, v190, v207 op_sel:[0,1,0] op_sel_hi:[0,1,0]
	v_fma_mix_f32 v206, v198, v191, v206 op_sel_hi:[0,1,0]
	v_fma_mix_f32 v207, v199, v191, v207 op_sel:[0,1,0] op_sel_hi:[0,1,0]
	v_cvt_f32_f16_e32 v13, v188
	v_cvt_f32_f16_sdwa v15, v188 dst_sel:DWORD dst_unused:UNUSED_PAD src0_sel:WORD_1
	ds_write_b128 v12, v[188:191]
	v_mov_b32_e32 v12, v59
	v_cvt_f32_f16_sdwa v18, v190 dst_sel:DWORD dst_unused:UNUSED_PAD src0_sel:WORD_1
	v_cvt_pk_fp8_f32 v12, v13, v15
	v_cvt_f32_f16_e32 v15, v190
	v_cvt_f32_f16_e32 v16, v189
	v_cvt_f32_f16_sdwa v17, v189 dst_sel:DWORD dst_unused:UNUSED_PAD src0_sel:WORD_1
	v_mov_b32_e32 v13, v59
	v_lshrrev_b32_e32 v14, 5, v62
	v_cvt_f32_f16_e32 v19, v191
	v_cvt_f32_f16_sdwa v20, v191 dst_sel:DWORD dst_unused:UNUSED_PAD src0_sel:WORD_1
	v_cvt_pk_fp8_f32 v13, v15, v18
	v_sub_u32_e32 v14, v14, v72
	v_cvt_pk_fp8_f32 v12, v16, v17 op_sel:[0,0,1]
	v_lshlrev_b32_e32 v16, 1, v14
	v_lshrrev_b32_e32 v15, 1, v14
	v_and_b32_e32 v16, 12, v16
	v_bfe_u32 v14, v14, 3, 2
	v_cvt_pk_fp8_f32 v13, v19, v20 op_sel:[0,0,1]
	v_bitop3_b32 v14, v16, v71, v14 bitop3:0x36
	v_add_lshl_u32 v15, v15, v70, 8
	v_lshlrev_b32_e32 v14, 4, v14
	v_or3_b32 v14, v15, v14, v1
	v_add_u32_e32 v14, 0x23800, v14
	v_add_f32_e32 v200, v200, v201
	v_add_f32_e32 v202, v202, v203
	v_add_f32_e32 v204, v204, v205
	v_add_f32_e32 v206, v206, v207
	v_lshlrev_b32_e32 v208, 7, v119
	v_lshl_add_u32 v208, v99, 2, v208
	v_add_u32_e32 v208, 0x27800, v208
	v_add_f32_dpp v200, v200, v200 quad_perm:[1,0,3,2] row_mask:0xf bank_mask:0xf
	v_add_f32_dpp v202, v202, v202 quad_perm:[1,0,3,2] row_mask:0xf bank_mask:0xf
	v_add_f32_dpp v204, v204, v204 quad_perm:[1,0,3,2] row_mask:0xf bank_mask:0xf
	v_add_f32_dpp v206, v206, v206 quad_perm:[1,0,3,2] row_mask:0xf bank_mask:0xf
	v_add_f32_dpp v200, v200, v200 quad_perm:[2,3,0,1] row_mask:0xf bank_mask:0xf
	v_add_f32_dpp v202, v202, v202 quad_perm:[2,3,0,1] row_mask:0xf bank_mask:0xf
	v_add_f32_dpp v204, v204, v204 quad_perm:[2,3,0,1] row_mask:0xf bank_mask:0xf
	v_add_f32_dpp v206, v206, v206 quad_perm:[2,3,0,1] row_mask:0xf bank_mask:0xf
	v_add_f32_dpp v200, v200, v200 row_half_mirror row_mask:0xf bank_mask:0xf
	v_add_f32_dpp v202, v202, v202 row_half_mirror row_mask:0xf bank_mask:0xf
	v_add_f32_dpp v204, v204, v204 row_half_mirror row_mask:0xf bank_mask:0xf
	v_add_f32_dpp v206, v206, v206 row_half_mirror row_mask:0xf bank_mask:0xf
	v_add_f32_dpp v200, v200, v200 row_mirror row_mask:0xf bank_mask:0xf
	v_add_f32_dpp v202, v202, v202 row_mirror row_mask:0xf bank_mask:0xf
	v_add_f32_dpp v204, v204, v204 row_mirror row_mask:0xf bank_mask:0xf
	v_add_f32_dpp v206, v206, v206 row_mirror row_mask:0xf bank_mask:0xf
	v_add_f32_dpp v200, v200, v200 row_bcast:15 row_mask:0xa bank_mask:0xf
	v_add_f32_dpp v202, v202, v202 row_bcast:15 row_mask:0xa bank_mask:0xf
	v_add_f32_dpp v204, v204, v204 row_bcast:15 row_mask:0xa bank_mask:0xf
	v_add_f32_dpp v206, v206, v206 row_bcast:15 row_mask:0xa bank_mask:0xf
	s_mov_b32 exec_lo, 0xffff0000
	s_mov_b32 exec_hi, 0xffff0000
	ds_write_b32 v208, v200
	ds_write_b32 v208, v202 offset:32
	ds_write_b32 v208, v204 offset:64
	ds_write_b32 v208, v206 offset:96
	s_mov_b64 exec, -1
	v_cmp_lt_i32_e32 vcc, v121, v60
	ds_write_b64 v14, v[12:13]
	v_mov_b32_e32 v15, v59
	v_cndmask_b32_e64 v12, 32, 0, vcc
	v_add_u32_e32 v16, v12, v121
	v_or_b32_e32 v12, v16, v101
	v_lshlrev_b32_e32 v58, 1, v12
	v_lshrrev_b32_e32 v12, 5, v0
	v_and_b32_e32 v12, 2, v12
	v_bitop3_b32 v14, v102, v100, v12 bitop3:0x36
	v_lshl_add_u64 v[12:13], v[10:11], 0, v[58:59]
	v_lshlrev_b64 v[12:13], 9, v[12:13]
	v_lshlrev_b32_e32 v16, 8, v16
	v_lshl_add_u64 v[12:13], s[4:5], 0, v[12:13]
	v_lshlrev_b32_e32 v14, 4, v14
	v_readfirstlane_b32 s6, v16
	v_add_u32_e32 v17, 0xc000, v16
	v_lshl_add_u64 v[12:13], v[12:13], 0, v[14:15]
	s_mov_b32 m0, s6
	s_mov_b64 s[6:7], 0x100
	v_readfirstlane_b32 s12, v17
	global_load_lds_dwordx4 v[12:13], off
	v_lshl_add_u64 v[12:13], v[12:13], 0, s[6:7]
	s_mov_b32 m0, s12
	v_or_b32_e32 v58, 1, v58
	global_load_lds_dwordx4 v[12:13], off
	v_lshl_add_u64 v[12:13], v[10:11], 0, v[58:59]
	v_lshlrev_b64 v[12:13], 9, v[12:13]
	v_lshl_add_u64 v[12:13], s[4:5], 0, v[12:13]
	v_lshl_add_u64 v[12:13], v[12:13], 0, v[14:15]
	v_add_u32_e32 v14, 0x6000, v16
	v_bfe_u32 v61, v0, 2, 2
	v_readfirstlane_b32 s12, v14
	v_add_u32_e32 v14, 0x12000, v16
	s_mov_b32 m0, s12
	v_readfirstlane_b32 s12, v14
	global_load_lds_dwordx4 v[12:13], off
	v_lshl_add_u64 v[12:13], v[12:13], 0, s[6:7]
	s_mov_b32 m0, s12
	v_add_u32_e32 v18, 0x23800, v117
	global_load_lds_dwordx4 v[12:13], off
	v_or_b32_e32 v12, 4, v121
	v_cmp_lt_i32_e32 vcc, v12, v60
	s_nop 1
	v_cndmask_b32_e64 v13, 32, 0, vcc
	v_add_u32_e32 v16, v13, v12
	v_or_b32_e32 v13, v16, v101
	v_lshlrev_b32_e32 v58, 1, v13
	v_bfe_u32 v12, v12, 2, 2
	v_bitop3_b32 v14, v102, v100, v12 bitop3:0x36
	v_lshl_add_u64 v[12:13], v[10:11], 0, v[58:59]
	v_lshlrev_b64 v[12:13], 9, v[12:13]
	v_lshlrev_b32_e32 v16, 8, v16
	v_lshl_add_u64 v[12:13], s[4:5], 0, v[12:13]
	v_lshlrev_b32_e32 v14, 4, v14
	v_readfirstlane_b32 s12, v16
	v_add_u32_e32 v17, 0xc000, v16
	v_lshl_add_u64 v[12:13], v[12:13], 0, v[14:15]
	s_mov_b32 m0, s12
	v_readfirstlane_b32 s12, v17
	v_or_b32_e32 v58, 1, v58
	global_load_lds_dwordx4 v[12:13], off
	v_lshl_add_u64 v[12:13], v[12:13], 0, s[6:7]
	s_mov_b32 m0, s12
	v_lshl_add_u64 v[10:11], v[10:11], 0, v[58:59]
	global_load_lds_dwordx4 v[12:13], off
	v_lshlrev_b64 v[10:11], 9, v[10:11]
	v_add_u32_e32 v12, 0x6000, v16
	v_lshl_add_u64 v[10:11], s[4:5], 0, v[10:11]
	v_readfirstlane_b32 s4, v12
	v_add_u32_e32 v12, 0x12000, v16
	v_lshl_add_u64 v[10:11], v[10:11], 0, v[14:15]
	s_mov_b32 m0, s4
	v_readfirstlane_b32 s4, v12
	global_load_lds_dwordx4 v[10:11], off
	v_lshl_add_u64 v[10:11], v[10:11], 0, s[6:7]
	s_mov_b32 m0, s4
	s_nop 0
	global_load_lds_dwordx4 v[10:11], off
	s_waitcnt lgkmcnt(0)
	s_barrier
	v_lshlrev_b32_e32 v10, 2, v0
	v_and_b32_e32 v94, 12, v10
	v_or_b32_e32 v120, v94, v61
	v_bitop3_b32 v10, v124, v94, v61 bitop3:0x1e
	v_lshl_or_b32 v14, v10, 4, v18
	v_bitop3_b32 v10, v124, v120, 1 bitop3:0x36
	v_lshl_or_b32 v19, v10, 4, v18
	s_load_dwordx4 s[4:7], s[0:1], 0x20
	s_load_dwordx2 s[12:13], s[0:1], 0x38
	ds_read_b128 v[10:13], v14
	ds_read_b128 v[62:65], v14 offset:8192
	ds_read_b128 v[14:17], v19
	ds_read_b128 v[66:69], v19 offset:8192
	v_bitop3_b32 v19, v124, v120, 4 bitop3:0x36
	v_lshl_or_b32 v19, v19, 4, v18
	v_bitop3_b32 v20, v124, v120, 5 bitop3:0x36
	v_lshl_or_b32 v20, v20, 4, v18
	ds_read_b128 v[70:73], v19
	ds_read_b128 v[78:81], v19 offset:8192
	ds_read_b128 v[74:77], v20
	ds_read_b128 v[82:85], v20 offset:8192
	v_bitop3_b32 v19, v124, v120, 8 bitop3:0x36
	v_lshl_or_b32 v19, v19, 4, v18
	v_bitop3_b32 v20, v124, v120, 9 bitop3:0x36
	v_lshl_or_b32 v20, v20, 4, v18
	ds_read_b128 v[86:89], v19
	ds_read_b128 v[104:107], v19 offset:8192
	ds_read_b128 v[90:93], v20
	ds_read_b128 v[108:111], v20 offset:8192
	v_bitop3_b32 v19, v124, v120, 12 bitop3:0x36
	v_lshl_or_b32 v19, v19, 4, v18
	v_bitop3_b32 v20, v124, v120, 13 bitop3:0x36
	v_lshl_or_b32 v18, v20, 4, v18
	ds_read_b128 v[126:129], v19
	ds_read_b128 v[134:137], v19 offset:8192
	ds_read_b128 v[130:133], v18
	ds_read_b128 v[138:141], v18 offset:8192
	v_mov_b32_e32 v103, 0x7f
	v_lshlrev_b32_e32 v58, 7, v99
	v_or_b32_e32 v122, 0x18000, v117
	s_waitcnt vmcnt(8) lgkmcnt(0)
	v_mfma_scale_f32_32x32x64_f8f6f4 v[18:33], v[2:9], v[10:17], 0, v103, v103 op_sel_hi:[0,0,0]
	v_lshlrev_b32_e32 v125, 3, v119
	v_or_b32_e32 v123, 0x1a000, v117
	v_mfma_scale_f32_32x32x64_f8f6f4 v[2:17], v[2:9], v[62:69], 0, v103, v103 op_sel_hi:[0,0,0]
	v_and_b32_e32 v62, 12, v95
	v_mfma_scale_f32_32x32x64_f8f6f4 v[18:33], v[50:57], v[70:77], v[18:33], v103, v103 op_sel_hi:[0,0,0]
	v_mfma_scale_f32_32x32x64_f8f6f4 v[2:17], v[50:57], v[78:85], v[2:17], v103, v103 op_sel_hi:[0,0,0]
	v_lshl_add_u64 v[50:51], s[10:11], 0, v[58:59]
	v_lshlrev_b32_e32 v58, 4, v119
	v_lshl_add_u64 v[54:55], v[50:51], 0, v[58:59]
	global_load_dwordx4 v[50:53], v[54:55], off
	s_brev_b32 s10, 60
	v_lshlrev_b32_e32 v58, 6, v0
	v_and_b32_e32 v58, 0x4000, v58
	v_or3_b32 v63, v122, v58, v125
	v_or3_b32 v58, v123, v58, v125
	v_mfma_scale_f32_32x32x64_f8f6f4 v[18:33], v[42:49], v[86:93], v[18:33], v103, v103 op_sel_hi:[0,0,0]
	v_mfma_scale_f32_32x32x64_f8f6f4 v[2:17], v[42:49], v[104:111], v[2:17], v103, v103 op_sel_hi:[0,0,0]
	global_load_dwordx4 v[42:45], v[54:55], off offset:32
	global_load_dwordx4 v[46:49], v[54:55], off offset:64
	s_nop 0
	global_load_dwordx4 v[54:57], v[54:55], off offset:96
	v_mfma_scale_f32_32x32x64_f8f6f4 v[2:17], v[34:41], v[134:141], v[2:17], v103, v103 op_sel_hi:[0,0,0]
	v_mfma_scale_f32_32x32x64_f8f6f4 v[18:33], v[34:41], v[126:133], v[18:33], v103, v103 op_sel_hi:[0,0,0]
	s_waitcnt vmcnt(0)
	s_nop 15
	s_nop 1
	v_fma_f32 v2, v2, s10, v50
	v_fma_f32 v3, v3, s10, v51
	v_fma_f32 v4, v4, s10, v52
	v_fma_f32 v5, v5, s10, v53
	v_cvt_pk_f16_f32 v2, v2, v3
	v_cvt_pk_f16_f32 v3, v4, v5
	v_bitop3_b32 v4, v95, v120, 12 bitop3:0x6c
	v_pk_fma_f32 v[18:19], v[18:19], s[10:11], v[50:51] op_sel_hi:[1,0,1]
	v_pk_fma_f32 v[20:21], v[20:21], s[10:11], v[52:53] op_sel_hi:[1,0,1]
	v_lshlrev_b32_e32 v4, 4, v4
	v_cvt_pk_f16_f32 v18, v18, v19
	v_cvt_pk_f16_f32 v19, v20, v21
	v_or_b32_e32 v5, v63, v4
	v_or_b32_e32 v4, v58, v4
	ds_write_b64 v5, v[18:19]
	ds_write_b64 v4, v[2:3]
	v_pk_fma_f32 v[2:3], v[22:23], s[10:11], v[42:43] op_sel_hi:[1,0,1]
	v_pk_fma_f32 v[4:5], v[6:7], s[10:11], v[42:43] op_sel_hi:[1,0,1]
	v_pk_fma_f32 v[6:7], v[24:25], s[10:11], v[44:45] op_sel_hi:[1,0,1]
	v_cvt_pk_f16_f32 v2, v2, v3
	v_cvt_pk_f16_f32 v3, v6, v7
	v_pk_fma_f32 v[6:7], v[8:9], s[10:11], v[44:45] op_sel_hi:[1,0,1]
	v_cvt_pk_f16_f32 v4, v4, v5
	v_cvt_pk_f16_f32 v5, v6, v7
	v_bitop3_b32 v6, v62, v120, 1 bitop3:0x36
	v_lshlrev_b32_e32 v6, 4, v6
	v_or_b32_e32 v7, v63, v6
	ds_write_b64 v7, v[2:3]
	v_or_b32_e32 v2, v58, v6
	ds_write_b64 v2, v[4:5]
	v_pk_fma_f32 v[2:3], v[26:27], s[10:11], v[46:47] op_sel_hi:[1,0,1]
	v_pk_fma_f32 v[6:7], v[28:29], s[10:11], v[48:49] op_sel_hi:[1,0,1]
	v_cvt_pk_f16_f32 v2, v2, v3
	v_pk_fma_f32 v[4:5], v[10:11], s[10:11], v[46:47] op_sel_hi:[1,0,1]
	v_cvt_pk_f16_f32 v3, v6, v7
	v_pk_fma_f32 v[6:7], v[12:13], s[10:11], v[48:49] op_sel_hi:[1,0,1]
	v_cvt_pk_f16_f32 v4, v4, v5
	v_cvt_pk_f16_f32 v5, v6, v7
	v_bitop3_b32 v6, v62, v120, 2 bitop3:0x36
	v_lshlrev_b32_e32 v6, 4, v6
	v_or_b32_e32 v7, v63, v6
	ds_write_b64 v7, v[2:3]
	v_or_b32_e32 v2, v58, v6
	ds_write_b64 v2, v[4:5]
	v_pk_fma_f32 v[2:3], v[30:31], s[10:11], v[54:55] op_sel_hi:[1,0,1]
	v_pk_fma_f32 v[6:7], v[32:33], s[10:11], v[56:57] op_sel_hi:[1,0,1]
	v_cvt_pk_f16_f32 v2, v2, v3
	v_pk_fma_f32 v[4:5], v[14:15], s[10:11], v[54:55] op_sel_hi:[1,0,1]
	v_cvt_pk_f16_f32 v3, v6, v7
	v_pk_fma_f32 v[6:7], v[16:17], s[10:11], v[56:57] op_sel_hi:[1,0,1]
	v_cvt_pk_f16_f32 v4, v4, v5
	v_cvt_pk_f16_f32 v5, v6, v7
	v_bitop3_b32 v6, v62, v120, 3 bitop3:0x36
	v_lshlrev_b32_e32 v6, 4, v6
	v_or_b32_e32 v7, v63, v6
	ds_write_b64 v7, v[2:3]
	v_or_b32_e32 v2, v58, v6
	ds_write_b64 v2, v[4:5]
	v_lshlrev_b32_e32 v2, 8, v101
	s_waitcnt lgkmcnt(0)
	s_barrier
	v_lshrrev_b32_e32 v27, 8, v0
	v_lshrrev_b32_e32 v3, 3, v0
	v_and_b32_e32 v3, 16, v3
	v_mul_u32_u24_e32 v28, 0x60, v27
	v_lshlrev_b32_e32 v26, 5, v27
	v_or_b32_e32 v146, v3, v100
	v_or_b32_e32 v147, v28, v100
	v_or_b32_e32 v4, v146, v26
	v_lshlrev_b32_e32 v209, 2, v4
	v_add_u32_e32 v209, 0x27800, v209
	v_or_b32_e32 v3, v147, v3
	v_lshlrev_b32_e32 v4, 8, v4
	v_add_u32_e32 v3, v3, v60
	v_or_b32_e32 v5, 0x18000, v4
	v_bitop3_b32 v11, v101, v120, 12 bitop3:0x36
	v_or_b32_e32 v95, 0x1c000, v4
	v_lshlrev_b32_e32 v29, 3, v101
	v_lshlrev_b32_e32 v4, 8, v3
	v_lshlrev_b32_e32 v12, 2, v3
	v_bfe_u32 v3, v3, 2, 2
	v_bitop3_b32 v6, v101, v94, v61 bitop3:0x1e
	v_bitop3_b32 v8, v101, v120, 4 bitop3:0x36
	v_bitop3_b32 v10, v101, v120, 8 bitop3:0x36
	v_lshlrev_b32_e32 v94, 4, v11
	v_and_b32_e32 v11, 8, v29
	v_and_or_b32 v3, v12, 12, v3
	v_lshlrev_b32_e32 v6, 4, v6
	v_lshlrev_b32_e32 v8, 4, v8
	v_lshlrev_b32_e32 v58, 4, v10
	v_mad_u32_u24 v4, v119, s17, v4
	v_bitop3_b32 v12, v11, v3, 1 bitop3:0x36
	v_bitop3_b32 v13, v11, v3, 2 bitop3:0x36
	v_bitop3_b32 v14, v11, v3, 3 bitop3:0x36
	v_bitop3_b32 v15, v11, v3, 4 bitop3:0x36
	v_bitop3_b32 v16, v11, v3, 5 bitop3:0x36
	v_bitop3_b32 v17, v11, v3, 6 bitop3:0x36
	v_or_b32_e32 v7, v5, v6
	v_or_b32_e32 v9, v5, v8
	v_or_b32_e32 v10, v5, v58
	v_or_b32_e32 v5, v5, v94
	v_or_b32_e32 v6, v95, v6
	v_or_b32_e32 v60, v95, v8
	v_bitop3_b32 v8, v29, v3, 8 bitop3:0x6c
	v_bitop3_b32 v2, v11, v3, 7 bitop3:0x36
	v_lshl_or_b32 v112, v12, 4, v4
	v_lshl_or_b32 v126, v13, 4, v4
	v_lshl_or_b32 v130, v14, 4, v4
	v_lshl_or_b32 v134, v15, 4, v4
	v_lshl_or_b32 v138, v16, 4, v4
	v_lshl_or_b32 v142, v17, 4, v4
	v_lshl_or_b32 v103, v8, 4, v4
	v_lshl_or_b32 v148, v2, 4, v4
	ds_read_b128 v[22:25], v7
	ds_read_b128 v[18:21], v9
	ds_read_b128 v[14:17], v10
	ds_read_b128 v[10:13], v5
	ds_read_b128 v[6:9], v6
	ds_read_b128 v[2:5], v60
	v_bfe_u32 v103, v0, 6, 1
	s_movk_i32 s5, 0x2000
	v_mbcnt_lo_u32_b32 v30, -1, 0
	v_mbcnt_hi_u32_b32 v32, -1, v30
	v_and_b32_e32 v33, 64, v32
	v_xor_b32_e32 v30, 16, v32
	v_add_u32_e32 v33, 64, v33
	v_cmp_lt_i32_e32 vcc, v30, v33
	v_mad_u32_u24 v44, v103, 48, v147
	v_lshlrev_b32_e32 v60, 8, v44
	v_cndmask_b32_e32 v30, v32, v30, vcc
	v_lshlrev_b32_e32 v30, 2, v30
	v_lshlrev_b32_e32 v44, 2, v44
	v_or_b32_e32 v35, v95, v58
	v_lshlrev_b32_e32 v58, 14, v99
	v_and_b32_e32 v44, 12, v44
	v_xor_b32_e32 v31, 32, v32
	v_cmp_lt_i32_e32 vcc, v31, v33
	v_or_b32_e32 v56, v44, v61
	v_bitop3_b32 v44, v101, v44, v61 bitop3:0x1e
	v_cndmask_b32_e32 v31, v32, v31, vcc
	v_lshl_add_u64 v[32:33], s[8:9], 0, v[58:59]
	v_lshlrev_b32_e32 v58, 4, v98
	v_or_b32_e32 v36, v95, v94
	v_lshl_add_u64 v[88:89], v[32:33], 0, v[58:59]
	v_lshl_or_b32 v57, v44, 4, v60
	ds_read_b128 v[40:43], v35
	ds_read_b128 v[106:109], v36
	s_load_dword s4, s[6:7], 0x0
	global_load_dwordx4 v[36:39], v[88:89], off
	global_load_dwordx4 v[32:35], v[88:89], off offset:1024
	ds_read_b128 v[44:47], v57
	v_bitop3_b32 v48, v101, v56, 4 bitop3:0x36
	v_lshl_or_b32 v62, v48, 4, v60
	ds_read_b128 v[48:51], v62
	v_bitop3_b32 v52, v101, v56, 8 bitop3:0x36
	v_lshl_or_b32 v63, v52, 4, v60
	ds_read_b128 v[52:55], v63
	s_waitcnt lgkmcnt(0)
	v_mfma_f32_16x16x32_f16 v[44:47], v[44:47], v[22:25], 0
	v_bitop3_b32 v64, v101, v56, 12 bitop3:0x36
	ds_read_b128 v[56:59], v57 offset:49152
	v_lshl_or_b32 v60, v64, 4, v60
	v_mfma_f32_16x16x32_f16 v[44:47], v[48:51], v[18:21], v[44:47]
	ds_read_b128 v[68:71], v60
	ds_read_b128 v[72:75], v62 offset:49152
	v_mad_u32_u24 v104, v103, 3, 1
	v_lshlrev_b32_e32 v132, 4, v104
	v_mfma_f32_16x16x32_f16 v[44:47], v[52:55], v[14:17], v[44:47]
	v_add_u32_e32 v52, v132, v147
	global_load_dwordx4 v[64:67], v[88:89], off offset:2048
	global_load_dwordx4 v[48:51], v[88:89], off offset:3072
	ds_read_b128 v[76:79], v63 offset:49152
	ds_read_b128 v[80:83], v60 offset:49152
	s_waitcnt lgkmcnt(3)
	v_mfma_f32_16x16x32_f16 v[44:47], v[68:71], v[10:13], v[44:47]
	v_lshlrev_b32_e32 v60, 8, v52
	v_lshlrev_b32_e32 v52, 2, v52
	v_and_b32_e32 v52, 12, v52
	v_mfma_f32_16x16x32_f16 v[44:47], v[56:59], v[6:9], v[44:47]
	v_or_b32_e32 v62, v52, v61
	v_bitop3_b32 v52, v101, v52, v61 bitop3:0x1e
	v_lshl_or_b32 v63, v52, 4, v60
	s_waitcnt lgkmcnt(2)
	v_mfma_f32_16x16x32_f16 v[44:47], v[72:75], v[2:5], v[44:47]
	ds_read_b128 v[52:55], v63
	v_bitop3_b32 v56, v101, v62, 4 bitop3:0x36
	v_lshl_or_b32 v84, v56, 4, v60
	s_waitcnt lgkmcnt(2)
	v_mfma_f32_16x16x32_f16 v[44:47], v[76:79], v[40:43], v[44:47]
	ds_read_b128 v[56:59], v84
	v_bitop3_b32 v68, v101, v62, 8 bitop3:0x36
	v_lshl_or_b32 v85, v68, 4, v60
	s_waitcnt lgkmcnt(2)
	v_mfma_f32_16x16x32_f16 v[110:113], v[80:83], v[106:109], v[44:47]
	ds_read_b128 v[68:71], v63 offset:49152
	v_bitop3_b32 v62, v101, v62, 12 bitop3:0x36
	v_lshl_or_b32 v60, v62, 4, v60
	ds_read_b128 v[44:47], v85
	s_waitcnt lgkmcnt(3)
	v_mfma_f32_16x16x32_f16 v[52:55], v[52:55], v[22:25], 0
	ds_read_b128 v[72:75], v60
	ds_read_b128 v[76:79], v84 offset:49152
	v_mad_u32_u24 v105, v103, 3, 2
	v_lshlrev_b32_e32 v133, 4, v105
	s_waitcnt lgkmcnt(4)
	v_mfma_f32_16x16x32_f16 v[52:55], v[56:59], v[18:21], v[52:55]
	ds_read_b128 v[56:59], v85 offset:49152
	v_add_co_u32_e32 v114, vcc, s15, v88
	s_waitcnt lgkmcnt(3)
	v_mfma_f32_16x16x32_f16 v[44:47], v[44:47], v[14:17], v[52:55]
	v_addc_co_u32_e32 v115, vcc, 0, v89, vcc
	v_lshlrev_b32_e32 v31, 2, v31
	s_waitcnt lgkmcnt(2)
	v_mfma_f32_16x16x32_f16 v[44:47], v[72:75], v[10:13], v[44:47]
	ds_read_b128 v[52:55], v60 offset:49152
	v_add_u32_e32 v60, v133, v147
	v_lshlrev_b32_e32 v72, 8, v60
	v_lshlrev_b32_e32 v60, 2, v60
	v_mfma_f32_16x16x32_f16 v[44:47], v[68:71], v[6:9], v[44:47]
	v_and_b32_e32 v60, 12, v60
	v_or_b32_e32 v68, v60, v61
	v_bitop3_b32 v60, v101, v60, v61 bitop3:0x1e
	v_lshl_or_b32 v69, v60, 4, v72
	s_waitcnt lgkmcnt(2)
	v_mfma_f32_16x16x32_f16 v[44:47], v[76:79], v[2:5], v[44:47]
	ds_read_b128 v[60:63], v69
	v_bitop3_b32 v70, v101, v68, 4 bitop3:0x36
	v_lshl_or_b32 v70, v70, 4, v72
	s_waitcnt lgkmcnt(2)
	v_mfma_f32_16x16x32_f16 v[44:47], v[56:59], v[40:43], v[44:47]
	ds_read_b128 v[56:59], v70
	v_bitop3_b32 v71, v101, v68, 8 bitop3:0x36
	v_lshl_or_b32 v71, v71, 4, v72
	s_waitcnt lgkmcnt(1)
	v_mfma_f32_16x16x32_f16 v[22:25], v[60:63], v[22:25], 0
	v_bitop3_b32 v60, v101, v68, 12 bitop3:0x36
	v_lshl_or_b32 v68, v60, 4, v72
	ds_read_b32 v210, v209
	v_mfma_f32_16x16x32_f16 v[126:129], v[52:55], v[106:109], v[44:47]
	s_nop 2
	ds_read_b128 v[44:47], v71
	ds_read_b128 v[52:55], v69 offset:49152
	ds_read_b128 v[60:63], v70 offset:49152
	s_waitcnt lgkmcnt(4)
	v_mfma_f32_16x16x32_f16 v[18:21], v[56:59], v[18:21], v[22:25]
	ds_read_b128 v[56:59], v71 offset:49152
	s_nop 1
	ds_read_b128 v[22:25], v68
	s_waitcnt lgkmcnt(4)
	v_mfma_f32_16x16x32_f16 v[14:17], v[44:47], v[14:17], v[18:21]
	v_add_co_u32_e32 v44, vcc, s5, v88
	s_movk_i32 s5, 0x3000
	s_nop 0
	ds_read_b128 v[18:21], v68 offset:49152
	s_waitcnt lgkmcnt(1)
	v_mfma_f32_16x16x32_f16 v[10:13], v[22:25], v[10:13], v[14:17]
	v_addc_co_u32_e32 v45, vcc, 0, v89, vcc
	global_load_dwordx4 v[84:87], v[114:115], off offset:1024
	global_load_dwordx4 v[80:83], v[114:115], off offset:2048
	global_load_dwordx4 v[92:95], v[44:45], off offset:-4096
	global_load_dwordx4 v[76:79], v[44:45], off
	v_mfma_f32_16x16x32_f16 v[6:9], v[52:55], v[6:9], v[10:13]
	global_load_dwordx4 v[72:75], v[44:45], off offset:1024
	global_load_dwordx4 v[68:71], v[44:45], off offset:2048
	global_load_dwordx4 v[52:55], v[44:45], off offset:3072
	v_mov_b32_e32 v13, 0xff61b1e6
	v_mfma_f32_16x16x32_f16 v[2:5], v[60:63], v[2:5], v[6:9]
	s_nop 2
	v_add_co_u32_e32 v6, vcc, s5, v88
	v_mfma_f32_16x16x32_f16 v[2:5], v[56:59], v[40:43], v[2:5]
	s_nop 0
	v_addc_co_u32_e32 v7, vcc, 0, v89, vcc
	global_load_dwordx4 v[88:91], v[114:115], off offset:3072
	global_load_dwordx4 v[60:63], v[6:7], off
	global_load_dwordx4 v[56:59], v[6:7], off offset:1024
	global_load_dwordx4 v[44:47], v[6:7], off offset:2048
	global_load_dwordx4 v[40:43], v[6:7], off offset:3072
	s_waitcnt lgkmcnt(0)
	v_mfma_f32_16x16x32_f16 v[16:19], v[18:21], v[106:109], v[2:5]
	s_mov_b32 s5, 0xff61b1e6
	s_nop 0
	v_or_b32_e32 v3, s14, v146
	v_mov_b32_e32 v4, 0x7df
	v_med3_u32 v3, v3, 32, v4
	v_or_b32_e32 v4, v97, v102
	v_sub_u32_e32 v3, v4, v3
	v_add_f32_e32 v2, s4, v210
	v_add_u32_e32 v3, 32, v3
	v_mad_u32_u24 v4, v103, 48, v3
	s_movk_i32 s4, 0x41
	v_add_f32_e32 v5, v2, v110
	v_mul_f32_e32 v5, 0x3db8aa3b, v5
	v_cmp_gt_u32_e32 vcc, s4, v4
	v_add_u32_e32 v6, 1, v4
	v_add_f32_e32 v7, v2, v111
	v_cndmask_b32_e32 v5, v13, v5, vcc
	v_mul_f32_e32 v7, 0x3db8aa3b, v7
	v_cmp_gt_u32_e32 vcc, s4, v6
	v_add_u32_e32 v8, 2, v4
	v_add_f32_e32 v9, v2, v112
	v_cndmask_b32_e32 v6, v13, v7, vcc
	v_mul_f32_e32 v9, 0x3db8aa3b, v9
	v_cmp_gt_u32_e32 vcc, s4, v8
	v_add_u32_e32 v4, 3, v4
	v_max3_f32 v7, v5, s5, v6
	v_cndmask_b32_e32 v8, v13, v9, vcc
	v_add_f32_e32 v9, v2, v113
	v_mul_f32_e32 v9, 0x3db8aa3b, v9
	v_cmp_gt_u32_e32 vcc, s4, v4
	v_add_u32_e32 v11, v3, v132
	v_add_f32_e32 v12, v2, v127
	v_cndmask_b32_e32 v10, v13, v9, vcc
	v_max3_f32 v4, v7, v8, v10
	v_add_f32_e32 v7, v2, v126
	v_mul_f32_e32 v7, 0x3db8aa3b, v7
	v_cmp_gt_u32_e32 vcc, s4, v11
	v_add_u32_e32 v9, 1, v11
	v_mul_f32_e32 v12, 0x3db8aa3b, v12
	v_cndmask_b32_e32 v7, v13, v7, vcc
	v_cmp_gt_u32_e32 vcc, s4, v9
	v_add_f32_e32 v14, v2, v128
	v_mul_f32_e32 v14, 0x3db8aa3b, v14
	v_cndmask_b32_e32 v9, v13, v12, vcc
	v_add_u32_e32 v12, 2, v11
	v_cmp_gt_u32_e32 vcc, s4, v12
	v_add_u32_e32 v11, 3, v11
	v_add_u32_e32 v3, v3, v133
	v_cndmask_b32_e32 v12, v13, v14, vcc
	v_add_f32_e32 v14, v2, v129
	v_mul_f32_e32 v14, 0x3db8aa3b, v14
	v_cmp_gt_u32_e32 vcc, s4, v11
	v_add_f32_e32 v11, v2, v16
	v_mul_f32_e32 v11, 0x3db8aa3b, v11
	v_cndmask_b32_e32 v15, v13, v14, vcc
	v_cmp_gt_u32_e32 vcc, s4, v3
	v_add_u32_e32 v14, 1, v3
	v_add_f32_e32 v16, v2, v17
	v_cndmask_b32_e32 v11, v13, v11, vcc
	v_mul_f32_e32 v16, 0x3db8aa3b, v16
	v_cmp_gt_u32_e32 vcc, s4, v14
	v_add_f32_e32 v17, v2, v18
	v_max3_f32 v4, v4, v7, v9
	v_cndmask_b32_e32 v14, v13, v16, vcc
	v_add_u32_e32 v16, 2, v3
	v_mul_f32_e32 v17, 0x3db8aa3b, v17
	v_cmp_gt_u32_e32 vcc, s4, v16
	v_add_u32_e32 v3, 3, v3
	v_add_f32_e32 v2, v2, v19
	v_max3_f32 v4, v4, v12, v15
	v_cndmask_b32_e32 v16, v13, v17, vcc
	v_mul_f32_e32 v2, 0x3db8aa3b, v2
	v_cmp_gt_u32_e32 vcc, s4, v3
	v_max3_f32 v4, v4, v11, v14
	v_lshlrev_b32_e32 v126, 5, v99
	v_cndmask_b32_e32 v17, v13, v2, vcc
	v_max3_f32 v2, v4, v16, v17
	ds_bpermute_b32 v3, v30, v2
	v_lshlrev_b32_e32 v127, 2, v119
	v_lshrrev_b32_e32 v4, 7, v0
	v_cmp_gt_u32_e32 vcc, 16, v98
	s_waitcnt lgkmcnt(0)
	v_max_f32_e32 v3, v3, v3
	v_max_f32_e32 v2, v2, v3
	ds_bpermute_b32 v3, v31, v2
	s_waitcnt lgkmcnt(0)
	v_max_f32_e32 v3, v3, v3
	v_max_f32_e32 v13, v2, v3
	v_and_b32_e32 v2, 0x180, v0
	v_or_b32_e32 v2, 0x23400, v2
	v_lshlrev_b32_e32 v3, 2, v100
	s_and_saveexec_b64 s[4:5], vcc
	v_lshlrev_b32_e32 v18, 6, v103
	v_add3_u32 v18, v2, v18, v3
	ds_write_b32 v18, v13
	s_or_b64 exec, exec, s[4:5]
	v_lshlrev_b32_e32 v18, 4, v103
	v_bitop3_b32 v19, v18, 16, v100 bitop3:0x36
	v_lshl_add_u32 v2, v19, 2, v2
	s_waitcnt lgkmcnt(0)
	s_barrier
	ds_read_b32 v19, v2
	v_max_f32_e32 v13, v13, v13
	v_mul_u32_u24_e32 v20, 0xd00, v4
	s_load_dwordx2 s[0:1], s[0:1], 0x30
	v_or_b32_e32 v2, 1, v124
	s_waitcnt lgkmcnt(0)
	v_max_f32_e32 v19, v19, v19
	v_max_f32_e32 v19, v13, v19
	v_sub_f32_e32 v5, v5, v19
	v_exp_f32_e32 v5, v5
	v_sub_f32_e32 v6, v6, v19
	v_exp_f32_e32 v6, v6
	v_sub_f32_e32 v8, v8, v19
	v_mul_u32_u24_e32 v13, 0xd0, v100
	v_exp_f32_e32 v8, v8
	v_sub_f32_e32 v10, v10, v19
	v_add3_u32 v20, v13, v20, v29
	v_exp_f32_e32 v10, v10
	v_or_b32_e32 v22, 0x20000, v20
	v_add_f32_e32 v20, 0, v5
	v_add_f32_e32 v20, v20, v6
	v_add_f32_e32 v20, v20, v8
	v_add_f32_e32 v23, v20, v10
	v_cvt_pk_f16_f32 v21, v8, v10
	v_cvt_pk_f16_f32 v20, v5, v6
	v_mad_u32_u24 v5, v103, s16, v22
	ds_write_b64 v5, v[20:21]
	v_sub_f32_e32 v5, v7, v19
	v_exp_f32_e32 v5, v5
	v_sub_f32_e32 v6, v9, v19
	v_exp_f32_e32 v6, v6
	v_sub_f32_e32 v7, v12, v19
	v_exp_f32_e32 v7, v7
	v_sub_f32_e32 v8, v15, v19
	v_exp_f32_e32 v8, v8
	v_sub_f32_e32 v10, v11, v19
	v_add_f32_e32 v9, v23, v5
	v_exp_f32_e32 v10, v10
	v_sub_f32_e32 v11, v14, v19
	v_add_f32_e32 v9, v9, v6
	v_exp_f32_e32 v11, v11
	v_sub_f32_e32 v12, v16, v19
	v_add_f32_e32 v9, v9, v7
	v_exp_f32_e32 v12, v12
	v_sub_f32_e32 v14, v17, v19
	v_add_f32_e32 v9, v9, v8
	v_exp_f32_e32 v14, v14
	v_add_f32_e32 v9, v9, v10
	v_add_f32_e32 v9, v9, v11
	v_add_f32_e32 v9, v9, v12
	v_add_f32_e32 v9, v9, v14
	ds_bpermute_b32 v15, v30, v9
	v_cvt_pk_f16_f32 v7, v7, v8
	v_cvt_pk_f16_f32 v6, v5, v6
	v_lshl_add_u32 v5, v104, 5, v22
	ds_write_b64 v5, v[6:7]
	s_waitcnt lgkmcnt(1)
	v_add_f32_e32 v5, v9, v15
	ds_bpermute_b32 v6, v31, v5
	s_movk_i32 s7, 0xd00
	s_mov_b32 s6, 0x20000
	v_cvt_pk_f16_f32 v9, v12, v14
	v_cvt_pk_f16_f32 v8, v10, v11
	v_lshl_add_u32 v7, v105, 5, v22
	ds_write_b64 v7, v[8:9]
	s_and_saveexec_b64 s[4:5], vcc
	s_cbranch_execz .LBB1_4
	v_lshlrev_b32_e32 v4, 5, v4
	v_or_b32_e32 v7, v18, v100
	v_lshlrev_b32_e32 v4, 2, v4
	v_lshlrev_b32_e32 v7, 2, v7
	s_mov_b32 s8, 0x23600
	v_add3_u32 v4, v7, v4, s8
	s_waitcnt lgkmcnt(1)
	v_add_f32_e32 v5, v5, v6
	ds_write_b32 v4, v5

	.amdhsa_kernel _Z7na_mainPKDF16_PKhS0_PKfS4_S4_S4_Pf
		.amdhsa_group_segment_fixed_size 162048
		.amdhsa_private_segment_fixed_size 0
		.amdhsa_kernarg_size 64
		.amdhsa_user_sgpr_count 2
		.amdhsa_user_sgpr_dispatch_ptr 0
		.amdhsa_user_sgpr_queue_ptr 0
		.amdhsa_user_sgpr_kernarg_segment_ptr 1
		.amdhsa_user_sgpr_dispatch_id 0
		.amdhsa_user_sgpr_kernarg_preload_length 0
		.amdhsa_user_sgpr_kernarg_preload_offset 0
		.amdhsa_user_sgpr_private_segment_size 0
		.amdhsa_uses_dynamic_stack 0
		.amdhsa_enable_private_segment 0
		.amdhsa_system_sgpr_workgroup_id_x 1
		.amdhsa_system_sgpr_workgroup_id_y 0
		.amdhsa_system_sgpr_workgroup_id_z 0
		.amdhsa_system_sgpr_workgroup_info 0
		.amdhsa_system_vgpr_workitem_id 0
		.amdhsa_next_free_vgpr 211
		.amdhsa_next_free_sgpr 96
		.amdhsa_accum_offset 212
		.amdhsa_reserve_vcc 1
		.amdhsa_float_round_mode_32 0
		.amdhsa_float_round_mode_16_64 0
		.amdhsa_float_denorm_mode_32 3
		.amdhsa_float_denorm_mode_16_64 3
		.amdhsa_dx10_clamp 1
		.amdhsa_ieee_mode 1
		.amdhsa_fp16_overflow 0
		.amdhsa_tg_split 0
		.amdhsa_exception_fp_ieee_invalid_op 0
		.amdhsa_exception_fp_denorm_src 0
		.amdhsa_exception_fp_ieee_div_zero 0
		.amdhsa_exception_fp_ieee_overflow 0
		.amdhsa_exception_fp_ieee_underflow 0
		.amdhsa_exception_fp_ieee_inexact 0
		.amdhsa_exception_int_div_zero 0
	.end_amdhsa_kernel

amdhsa.kernels:
  - .agpr_count:     16
    .args:
      - .actual_access:  read_only
        .address_space:  global
        .offset:         0
        .size:           8
        .value_kind:     global_buffer
      - .actual_access:  read_only
        .address_space:  global
        .offset:         8
        .size:           8
        .value_kind:     global_buffer
      - .actual_access:  read_only
        .address_space:  global
        .offset:         16
        .size:           8
        .value_kind:     global_buffer
      - .actual_access:  read_only
        .address_space:  global
        .offset:         24
        .size:           8
        .value_kind:     global_buffer
      - .actual_access:  read_only
        .address_space:  global
        .offset:         32
        .size:           8
        .value_kind:     global_buffer
      - .actual_access:  read_only
        .address_space:  global
        .offset:         40
        .size:           8
        .value_kind:     global_buffer
      - .actual_access:  write_only
        .address_space:  global
        .offset:         48
        .size:           8
        .value_kind:     global_buffer
      - .actual_access:  write_only
        .address_space:  global
        .offset:         56
        .size:           8
        .value_kind:     global_buffer
      - .actual_access:  write_only
        .address_space:  global
        .offset:         64
        .size:           8
        .value_kind:     global_buffer
      - .actual_access:  write_only
        .address_space:  global
        .offset:         72
        .size:           8
        .value_kind:     global_buffer
      - .actual_access:  write_only
        .address_space:  global
        .offset:         80
        .size:           8
        .value_kind:     global_buffer
      - .actual_access:  write_only
        .address_space:  global
        .offset:         88
        .size:           8
        .value_kind:     global_buffer
    .group_segment_fixed_size: 16384
    .kernarg_segment_align: 8
    .kernarg_segment_size: 96
    .language:       OpenCL C
    .language_version:
      - 2
      - 0
    .max_flat_workgroup_size: 256
    .name:           _Z7na_prepPKfS0_S0_S0_S0_S0_PDF16_PhS1_PfS3_S3_
    .private_segment_fixed_size: 0
    .sgpr_count:     23
    .sgpr_spill_count: 0
    .symbol:         _Z7na_prepPKfS0_S0_S0_S0_S0_PDF16_PhS1_PfS3_S3_.kd
    .uniform_work_group_size: 1
    .uses_dynamic_stack: false
    .vgpr_count:     116
    .vgpr_spill_count: 0
    .wavefront_size: 64
  - .agpr_count:     0
    .args:
      - .address_space:  global
        .offset:         0
        .size:           8
        .value_kind:     global_buffer
      - .actual_access:  read_only
        .address_space:  global
        .offset:         8
        .size:           8
        .value_kind:     global_buffer
      - .actual_access:  read_only
        .address_space:  global
        .offset:         16
        .size:           8
        .value_kind:     global_buffer
      - .actual_access:  read_only
        .address_space:  global
        .offset:         24
        .size:           8
        .value_kind:     global_buffer
      - .actual_access:  read_only
        .address_space:  global
        .offset:         32
        .size:           8
        .value_kind:     global_buffer
      - .actual_access:  read_only
        .address_space:  global
        .offset:         40
        .size:           8
        .value_kind:     global_buffer
      - .actual_access:  read_only
        .address_space:  global
        .offset:         48
        .size:           8
        .value_kind:     global_buffer
      - .actual_access:  write_only
        .address_space:  global
        .offset:         56
        .size:           8
        .value_kind:     global_buffer
    .group_segment_fixed_size: 162048
    .kernarg_segment_align: 8
    .kernarg_segment_size: 64
    .language:       OpenCL C
    .language_version:
      - 2
      - 0
    .max_flat_workgroup_size: 512
    .name:           _Z7na_mainPKDF16_PKhS0_PKfS4_S4_S4_Pf
    .private_segment_fixed_size: 0
    .sgpr_count:     24
    .sgpr_spill_count: 0
    .symbol:         _Z7na_mainPKDF16_PKhS0_PKfS4_S4_S4_Pf.kd
    .uniform_work_group_size: 1
    .uses_dynamic_stack: false
    .vgpr_count:     211
    .vgpr_spill_count: 0
    .wavefront_size: 64
